# v13 + P8 router-logits f32-MFMA loop double-buffered: next k-slice operands loaded during the current slice's 16 MFMAs
# speedup vs baseline: 1.0082x; 1.0082x over previous
.LBB0_992:
	v_lshl_add_u64 v[24:25], v[20:21], 0, s[12:13]
	global_load_dwordx2 v[132:133], v[18:19], off offset:-32
	global_load_dwordx2 v[134:135], v[18:19], off offset:-16
	global_load_dwordx2 v[136:137], v[18:19], off
	global_load_dwordx2 v[138:139], v[18:19], off offset:16
	global_load_dword v140, v[24:25], off
	global_load_dword v141, v[24:25], off offset:128
	global_load_dword v142, v[24:25], off offset:256
	global_load_dword v143, v[24:25], off offset:384
	global_load_dword v144, v[24:25], off offset:1024
	global_load_dword v145, v[24:25], off offset:1152
	global_load_dword v146, v[24:25], off offset:1280
	global_load_dword v147, v[24:25], off offset:1408
	global_load_dword v148, v[24:25], off offset:2048
	global_load_dword v149, v[24:25], off offset:2176
	global_load_dword v150, v[24:25], off offset:2304
	global_load_dword v151, v[24:25], off offset:2432
	global_load_dword v152, v[24:25], off offset:3072
	global_load_dword v153, v[24:25], off offset:3200
	global_load_dword v154, v[24:25], off offset:3328
	global_load_dword v155, v[24:25], off offset:3456
	s_add_u32 s12, s12, 0x1000
	s_addc_u32 s13, s13, 0
	v_lshl_add_u64 v[18:19], v[18:19], 0, 64
.Lrt_loop:
	v_lshl_add_u64 v[24:25], v[20:21], 0, s[12:13]
	global_load_dwordx2 v[156:157], v[18:19], off offset:-32
	global_load_dwordx2 v[158:159], v[18:19], off offset:-16
	global_load_dwordx2 v[160:161], v[18:19], off
	global_load_dwordx2 v[162:163], v[18:19], off offset:16
	global_load_dword v164, v[24:25], off
	global_load_dword v165, v[24:25], off offset:128
	global_load_dword v166, v[24:25], off offset:256
	global_load_dword v167, v[24:25], off offset:384
	global_load_dword v168, v[24:25], off offset:1024
	global_load_dword v169, v[24:25], off offset:1152
	global_load_dword v170, v[24:25], off offset:1280
	global_load_dword v171, v[24:25], off offset:1408
	global_load_dword v172, v[24:25], off offset:2048
	global_load_dword v173, v[24:25], off offset:2176
	global_load_dword v174, v[24:25], off offset:2304
	global_load_dword v175, v[24:25], off offset:2432
	global_load_dword v176, v[24:25], off offset:3072
	global_load_dword v177, v[24:25], off offset:3200
	global_load_dword v178, v[24:25], off offset:3328
	global_load_dword v179, v[24:25], off offset:3456
	s_add_u32 s12, s12, 0x1000
	s_addc_u32 s13, s13, 0
	v_lshl_add_u64 v[18:19], v[18:19], 0, 64
	s_waitcnt vmcnt(20)
	v_lshlrev_b32_e32 v22, 16, v132
	v_and_b32_e32 v23, 0xffff0000, v132
	v_lshlrev_b32_e32 v26, 16, v133
	v_mfma_f32_32x32x2_f32 v[2:17], v22, v140, v[2:17]
	v_and_b32_e32 v27, 0xffff0000, v133
	v_mfma_f32_32x32x2_f32 v[2:17], v23, v141, v[2:17]
	v_lshlrev_b32_e32 v22, 16, v134
	v_mfma_f32_32x32x2_f32 v[2:17], v26, v142, v[2:17]
	v_and_b32_e32 v23, 0xffff0000, v134
	v_mfma_f32_32x32x2_f32 v[2:17], v27, v143, v[2:17]
	v_lshlrev_b32_e32 v26, 16, v135
	v_mfma_f32_32x32x2_f32 v[2:17], v22, v144, v[2:17]
	v_and_b32_e32 v27, 0xffff0000, v135
	v_mfma_f32_32x32x2_f32 v[2:17], v23, v145, v[2:17]
	v_lshlrev_b32_e32 v22, 16, v136
	v_mfma_f32_32x32x2_f32 v[2:17], v26, v146, v[2:17]
	v_and_b32_e32 v23, 0xffff0000, v136
	v_mfma_f32_32x32x2_f32 v[2:17], v27, v147, v[2:17]
	v_lshlrev_b32_e32 v26, 16, v137
	v_mfma_f32_32x32x2_f32 v[2:17], v22, v148, v[2:17]
	v_and_b32_e32 v27, 0xffff0000, v137
	v_mfma_f32_32x32x2_f32 v[2:17], v23, v149, v[2:17]
	v_lshlrev_b32_e32 v22, 16, v138
	v_mfma_f32_32x32x2_f32 v[2:17], v26, v150, v[2:17]
	v_and_b32_e32 v23, 0xffff0000, v138
	v_mfma_f32_32x32x2_f32 v[2:17], v27, v151, v[2:17]
	v_lshlrev_b32_e32 v26, 16, v139
	v_mfma_f32_32x32x2_f32 v[2:17], v22, v152, v[2:17]
	v_and_b32_e32 v27, 0xffff0000, v139
	v_mfma_f32_32x32x2_f32 v[2:17], v23, v153, v[2:17]
	v_mfma_f32_32x32x2_f32 v[2:17], v26, v154, v[2:17]
	v_mfma_f32_32x32x2_f32 v[2:17], v27, v155, v[2:17]
	s_cmp_eq_u32 s12, 0x10000
	s_cbranch_scc1 .Lrt_tail
	v_lshl_add_u64 v[24:25], v[20:21], 0, s[12:13]
	global_load_dwordx2 v[132:133], v[18:19], off offset:-32
	global_load_dwordx2 v[134:135], v[18:19], off offset:-16
	global_load_dwordx2 v[136:137], v[18:19], off
	global_load_dwordx2 v[138:139], v[18:19], off offset:16
	global_load_dword v140, v[24:25], off
	global_load_dword v141, v[24:25], off offset:128
	global_load_dword v142, v[24:25], off offset:256
	global_load_dword v143, v[24:25], off offset:384
	global_load_dword v144, v[24:25], off offset:1024
	global_load_dword v145, v[24:25], off offset:1152
	global_load_dword v146, v[24:25], off offset:1280
	global_load_dword v147, v[24:25], off offset:1408
	global_load_dword v148, v[24:25], off offset:2048
	global_load_dword v149, v[24:25], off offset:2176
	global_load_dword v150, v[24:25], off offset:2304
	global_load_dword v151, v[24:25], off offset:2432
	global_load_dword v152, v[24:25], off offset:3072
	global_load_dword v153, v[24:25], off offset:3200
	global_load_dword v154, v[24:25], off offset:3328
	global_load_dword v155, v[24:25], off offset:3456
	s_add_u32 s12, s12, 0x1000
	s_addc_u32 s13, s13, 0
	v_lshl_add_u64 v[18:19], v[18:19], 0, 64
	s_waitcnt vmcnt(20)
	v_lshlrev_b32_e32 v22, 16, v156
	v_and_b32_e32 v23, 0xffff0000, v156
	v_lshlrev_b32_e32 v26, 16, v157
	v_mfma_f32_32x32x2_f32 v[2:17], v22, v164, v[2:17]
	v_and_b32_e32 v27, 0xffff0000, v157
	v_mfma_f32_32x32x2_f32 v[2:17], v23, v165, v[2:17]
	v_lshlrev_b32_e32 v22, 16, v158
	v_mfma_f32_32x32x2_f32 v[2:17], v26, v166, v[2:17]
	v_and_b32_e32 v23, 0xffff0000, v158
	v_mfma_f32_32x32x2_f32 v[2:17], v27, v167, v[2:17]
	v_lshlrev_b32_e32 v26, 16, v159
	v_mfma_f32_32x32x2_f32 v[2:17], v22, v168, v[2:17]
	v_and_b32_e32 v27, 0xffff0000, v159
	v_mfma_f32_32x32x2_f32 v[2:17], v23, v169, v[2:17]
	v_lshlrev_b32_e32 v22, 16, v160
	v_mfma_f32_32x32x2_f32 v[2:17], v26, v170, v[2:17]
	v_and_b32_e32 v23, 0xffff0000, v160
	v_mfma_f32_32x32x2_f32 v[2:17], v27, v171, v[2:17]
	v_lshlrev_b32_e32 v26, 16, v161
	v_mfma_f32_32x32x2_f32 v[2:17], v22, v172, v[2:17]
	v_and_b32_e32 v27, 0xffff0000, v161
	v_mfma_f32_32x32x2_f32 v[2:17], v23, v173, v[2:17]
	v_lshlrev_b32_e32 v22, 16, v162
	v_mfma_f32_32x32x2_f32 v[2:17], v26, v174, v[2:17]
	v_and_b32_e32 v23, 0xffff0000, v162
	v_mfma_f32_32x32x2_f32 v[2:17], v27, v175, v[2:17]
	v_lshlrev_b32_e32 v26, 16, v163
	v_mfma_f32_32x32x2_f32 v[2:17], v22, v176, v[2:17]
	v_and_b32_e32 v27, 0xffff0000, v163
	v_mfma_f32_32x32x2_f32 v[2:17], v23, v177, v[2:17]
	v_mfma_f32_32x32x2_f32 v[2:17], v26, v178, v[2:17]
	v_mfma_f32_32x32x2_f32 v[2:17], v27, v179, v[2:17]
	s_branch .Lrt_loop
.Lrt_tail:
	s_waitcnt vmcnt(0)
	v_lshlrev_b32_e32 v22, 16, v156
	v_and_b32_e32 v23, 0xffff0000, v156
	v_lshlrev_b32_e32 v26, 16, v157
	v_mfma_f32_32x32x2_f32 v[2:17], v22, v164, v[2:17]
	v_and_b32_e32 v27, 0xffff0000, v157
	v_mfma_f32_32x32x2_f32 v[2:17], v23, v165, v[2:17]
	v_lshlrev_b32_e32 v22, 16, v158
	v_mfma_f32_32x32x2_f32 v[2:17], v26, v166, v[2:17]
	v_and_b32_e32 v23, 0xffff0000, v158
	v_mfma_f32_32x32x2_f32 v[2:17], v27, v167, v[2:17]
	v_lshlrev_b32_e32 v26, 16, v159
	v_mfma_f32_32x32x2_f32 v[2:17], v22, v168, v[2:17]
	v_and_b32_e32 v27, 0xffff0000, v159
	v_mfma_f32_32x32x2_f32 v[2:17], v23, v169, v[2:17]
	v_lshlrev_b32_e32 v22, 16, v160
	v_mfma_f32_32x32x2_f32 v[2:17], v26, v170, v[2:17]
	v_and_b32_e32 v23, 0xffff0000, v160
	v_mfma_f32_32x32x2_f32 v[2:17], v27, v171, v[2:17]
	v_lshlrev_b32_e32 v26, 16, v161
	v_mfma_f32_32x32x2_f32 v[2:17], v22, v172, v[2:17]
	v_and_b32_e32 v27, 0xffff0000, v161
	v_mfma_f32_32x32x2_f32 v[2:17], v23, v173, v[2:17]
	v_lshlrev_b32_e32 v22, 16, v162
	v_mfma_f32_32x32x2_f32 v[2:17], v26, v174, v[2:17]
	v_and_b32_e32 v23, 0xffff0000, v162
	v_mfma_f32_32x32x2_f32 v[2:17], v27, v175, v[2:17]
	v_lshlrev_b32_e32 v26, 16, v163
	v_mfma_f32_32x32x2_f32 v[2:17], v22, v176, v[2:17]
	v_and_b32_e32 v27, 0xffff0000, v163
	v_mfma_f32_32x32x2_f32 v[2:17], v23, v177, v[2:17]
	v_mfma_f32_32x32x2_f32 v[2:17], v26, v178, v[2:17]
	v_mfma_f32_32x32x2_f32 v[2:17], v27, v179, v[2:17]
	v_lshl_or_b32 v18, s2, 6, v66
	v_or_b32_e32 v18, s3, v18
	s_movk_i32 s2, 0x84
	v_mad_u64_u32 v[18:19], s[2:3], v18, s2, v[34:35]
	s_nop 12
	ds_write2_b32 v18, v2, v3 offset0:64 offset1:97
	ds_write2_b32 v18, v4, v5 offset0:130 offset1:163
	v_add_u32_e32 v2, 0x400, v18
	ds_write2_b32 v2, v6, v7 offset0:72 offset1:105
	ds_write2_b32 v2, v8, v9 offset0:138 offset1:171
	v_add_u32_e32 v2, 0x800, v18
	ds_write2_b32 v2, v10, v11 offset0:80 offset1:113
	ds_write2_b32 v2, v12, v13 offset0:146 offset1:179
	v_add_u32_e32 v2, 0xc00, v18
	ds_write2_b32 v2, v14, v15 offset0:88 offset1:121
	ds_write2_b32 v2, v16, v17 offset0:154 offset1:187
	s_mov_b64 s[2:3], 0
	v_mov_b32_e32 v2, v70
	v_mov_b32_e32 v3, v69
	v_mov_b32_e32 v4, v68
	s_waitcnt lgkmcnt(0)
	s_barrier
